# v_A_fixed plus: skip the grid barrier after the last GEMM phase on a 256-workgroup grid (the phase it guards is empty)
# speedup vs baseline: 1.0037x; 1.0017x over previous
.LBB0_1814:
	s_cmp_gt_i32 s95, 16
	s_cselect_b64 s[4:5], -1, 0
	s_and_b64 s[0:1], s[0:1], s[4:5]
	s_andn2_b64 vcc, exec, s[0:1]
	s_cbranch_vccnz .LBB0_1864
	v_readlane_b32 s98, v246, 17
	v_readlane_b32 s99, v246, 18
	s_and_b64 vcc, exec, s[98:99]
	s_cbranch_vccnz .LBB0_1864
	s_waitcnt vmcnt(0)
	v_cmp_eq_u32_e32 vcc, 0, v0
	s_waitcnt vmcnt(0)
	s_barrier
	s_and_saveexec_b64 s[0:1], vcc
	s_cbranch_execz .LBB0_1863
	v_readlane_b32 s46, v247, 40
	s_waitcnt vmcnt(0) expcnt(0) lgkmcnt(0)
	s_nop 0
	v_mov_b32_e32 v1, s46
	ds_read_b32 v3, v1
	ds_read_b32 v1, v1 offset:4
	s_waitcnt lgkmcnt(1)
	v_cmp_ne_u32_e32 vcc, 0, v3
	s_cbranch_vccnz .LBB0_1831
	v_readlane_b32 s6, v247, 0
	v_readlane_b32 s7, v247, 1
	s_load_dwordx2 s[10:11], s[6:7], 0x4
	s_add_u32 s6, s52, 0x4200
	s_addc_u32 s7, s53, 0
	s_add_u32 s8, s52, 0x4400
	s_addc_u32 s9, s53, 0
	s_waitcnt lgkmcnt(0)
	s_mul_i32 s3, s10, s33
	s_add_u32 s10, s52, 0x4500
	s_mul_i32 s3, s3, s11
	s_addc_u32 s11, s53, 0
	s_add_u32 s12, s52, 0x4600
	s_addc_u32 s13, s53, 0
	s_add_u32 s14, s52, 0x4700
	s_addc_u32 s15, s53, 0
	s_add_u32 s16, s52, 0x4800
	s_addc_u32 s17, s53, 0
	s_add_u32 s18, s52, 0x4900
	s_addc_u32 s19, s53, 0
	s_add_u32 s20, s52, 0x4a00
	s_addc_u32 s21, s53, 0
	s_add_u32 s22, s52, 0x4b00
	s_addc_u32 s23, s53, 0
	s_add_u32 s24, s52, 0x4c00
	s_addc_u32 s25, s53, 0
	s_add_u32 s26, s52, 0x4d00
	s_addc_u32 s27, s53, 0
	s_add_u32 s28, s52, 0x4e00
	s_addc_u32 s29, s53, 0
	s_add_u32 s30, s52, 0x4f00
	s_addc_u32 s31, s53, 0
	s_add_u32 s34, s52, 0x5000
	s_addc_u32 s35, s53, 0
	s_add_u32 s36, s52, 0x5100
	s_addc_u32 s37, s53, 0
	s_add_u32 s38, s52, 0x5200
	s_addc_u32 s39, s53, 0
	s_add_u32 s40, s52, 0x5300
	s_addc_u32 s41, s53, 0
	s_mov_b32 s33, 1
	v_mov_b32_e32 v17, 0
	s_branch .LBB0_1819
